# baseline (speedup 1.0000x reference)
_Z6scan_kPKDF16_S0_S0_S0_PKfPf:
	s_load_dwordx8 s[4:11], s[0:1], 0x0
	s_load_dwordx4 s[12:15], s[0:1], 0x20
	v_and_b32_e32 v1, 63, v0
	v_lshrrev_b32_e32 v2, 6, v0
	s_nop 1
	v_readfirstlane_b32 s16, v2
	s_lshr_b32 s17, s2, 7
	s_and_b32 s18, s2, 127
	s_lshl_b32 s18, s18, 2
	s_add_u32 s18, s18, s16
	s_lshl_b32 s19, s17, 9
	s_add_u32 s19, s19, s18
	s_mul_i32 s28, s16, 4608
	s_add_u32 s28, s28, 67584
	s_lshl_b32 s32, s16, 10
	s_add_u32 s33, s32, 0x1000
	s_add_u32 s34, s32, 0x2000
	s_add_u32 s35, s32, 0x3000
	s_mov_b32 s46, 0x200
	s_mov_b32 s47, 0
	s_mov_b32 s40, 0
	v_lshlrev_b32_e32 v2, 4, v1
	v_add_u32_e32 v3, 0x1000, v2
	v_add_u32_e32 v4, 0x2000, v2
	v_add_u32_e32 v5, 0x3000, v2
	v_lshlrev_b32_e32 v6, 2, v1
	v_lshlrev_b32_e32 v7, 1, v1
	v_and_b32_e32 v20, 7, v1
	v_lshlrev_b32_e32 v20, 1, v20
	v_add_u32_e32 v8, v2, v20
	v_add_u32_e32 v8, s28, v8
	v_and_b32_e32 v20, 3, v1
	v_bfe_u32 v21, v1, 3, 2
	v_lshl_add_u32 v20, v21, 2, v20
	v_lshrrev_b32_e32 v21, 5, v1
	v_bfe_u32 v22, v1, 2, 1
	v_bfe_u32 v23, v1, 4, 1
	v_cmp_eq_u32_e64 s[48:49], v21, v22
	v_cmp_eq_u32_e64 s[50:51], 0, v23
	s_nop 1
	s_and_b64 s[52:53], s[48:49], s[50:51]
	s_andn2_b64 s[54:55], s[48:49], s[50:51]
	v_mov_b32_e32 v24, 65536
	v_lshlrev_b32_e32 v25, 1, v20
	v_add_u32_e32 v25, s28, v25
	v_add_u32_e32 v26, 0x100, v25
	s_nop 1
	v_cndmask_b32_e64 v9, v24, v25, s[48:49]
	v_cndmask_b32_e64 v10, v24, v26, s[48:49]
	v_lshlrev_b32_e32 v25, 4, v20
	v_add_u32_e32 v25, s28, v25
	v_add_u32_e32 v25, 0x200, v25
	v_add_u32_e32 v26, 0x800, v25
	v_cndmask_b32_e64 v11, v24, v25, s[48:49]
	v_cndmask_b32_e64 v13, v24, v26, s[48:49]
	v_mov_b32_e32 v15, 1.0
	v_and_b32_e32 v89, 15, v1
	s_mov_b32 s42, 0xffff
	s_mov_b32 s43, 0
	v_xor_b32_e32 v86, 16, v1
	v_lshlrev_b32_e32 v86, 2, v86
	v_xor_b32_e32 v87, 32, v1
	v_lshlrev_b32_e32 v87, 2, v87
	s_waitcnt lgkmcnt(0)
	s_lshl_b32 s30, s19, 13
	s_add_u32 s24, s4, s30
	s_addc_u32 s25, s5, 0
	s_add_u32 s26, s6, s30
	s_addc_u32 s27, s7, 0
	s_lshl_b32 s30, s17, 19
	s_add_u32 s30, s30, s32
	s_add_u32 s20, s8, s30
	s_addc_u32 s21, s9, 0
	s_add_u32 s22, s10, s30
	s_addc_u32 s23, s11, 0
	s_lshl_b32 s30, s18, 8
	s_add_u32 s12, s12, s30
	s_addc_u32 s13, s13, 0
	global_load_dword v90, v6, s[12:13]
	global_load_ushort v18, v7, s[26:27]
	global_load_ushort v19, v7, s[26:27] offset:128
	s_lshl_b32 s30, s19, 14
	s_add_u32 s14, s14, s30
	s_addc_u32 s15, s15, 0
	v_and_b32_e32 v30, 15, v1
	v_lshlrev_b32_e32 v30, 2, v30
	v_mov_b32_e32 v31, 0
	v_lshl_add_u64 v[16:17], s[14:15], 0, v[30:31]
	v_mov_b32_e32 v36, 0
	v_mov_b32_e32 v37, 0
	v_mov_b32_e32 v38, 0
	v_mov_b32_e32 v39, 0
	v_add_u32_e32 v29, 65536, v2
	ds_write_b128 v29, v[36:39]
	ds_write_b128 v29, v[36:39] offset:1024
	v_add_u32_e32 v29, s28, v2
	ds_write_b128 v29, v[36:39] offset:512
	ds_write_b128 v29, v[36:39] offset:1536
	ds_write_b128 v29, v[36:39] offset:2560
	ds_write_b128 v29, v[36:39] offset:3584
	s_mov_b32 m0, s32
	s_nop 0
	global_load_lds_dwordx4 v2, s[20:21]
	s_add_i32 m0, s32, 32768
	s_nop 0
	global_load_lds_dwordx4 v2, s[22:23]
	s_mov_b32 m0, s33
	s_nop 0
	global_load_lds_dwordx4 v3, s[20:21]
	s_add_i32 m0, s33, 32768
	s_nop 0
	global_load_lds_dwordx4 v3, s[22:23]
	s_mov_b32 m0, s34
	s_nop 0
	global_load_lds_dwordx4 v4, s[20:21]
	s_add_i32 m0, s34, 32768
	s_nop 0
	global_load_lds_dwordx4 v4, s[22:23]
	s_mov_b32 m0, s35
	s_nop 0
	global_load_lds_dwordx4 v5, s[20:21]
	s_add_i32 m0, s35, 32768
	s_nop 0
	global_load_lds_dwordx4 v5, s[22:23]
	s_mov_b32 m0, s28
	s_nop 0
	global_load_lds_dword v6, s[24:25]
	s_add_u32 s20, s20, 0x4000
	s_addc_u32 s21, s21, 0
	s_add_u32 s22, s22, 0x4000
	s_addc_u32 s23, s23, 0
	s_add_u32 s24, s24, 0x100
	s_addc_u32 s25, s25, 0
	s_add_i32 m0, s32, 16384
	s_nop 0
	global_load_lds_dwordx4 v2, s[20:21]
	s_add_i32 m0, s32, 49152
	s_nop 0
	global_load_lds_dwordx4 v2, s[22:23]
	s_add_i32 m0, s33, 16384
	s_nop 0
	global_load_lds_dwordx4 v3, s[20:21]
	s_add_i32 m0, s33, 49152
	s_nop 0
	global_load_lds_dwordx4 v3, s[22:23]
	s_add_i32 m0, s34, 16384
	s_nop 0
	global_load_lds_dwordx4 v4, s[20:21]
	s_add_i32 m0, s34, 49152
	s_nop 0
	global_load_lds_dwordx4 v4, s[22:23]
	s_add_i32 m0, s35, 16384
	s_nop 0
	global_load_lds_dwordx4 v5, s[20:21]
	s_add_i32 m0, s35, 49152
	s_nop 0
	global_load_lds_dwordx4 v5, s[22:23]
	s_add_i32 m0, s28, 0x100
	s_nop 0
	global_load_lds_dword v6, s[24:25]
	s_add_u32 s20, s20, 0x4000
	s_addc_u32 s21, s21, 0
	s_add_u32 s22, s22, 0x4000
	s_addc_u32 s23, s23, 0
	s_add_u32 s24, s24, 0x100
	s_addc_u32 s25, s25, 0
	s_mov_b32 s3, 0x3fb8aa3b
	s_waitcnt vmcnt(20)
	v_mul_f32_e32 v91, 0x3fb8aa3b, v90
	v_fma_f32 v92, v90, s3, -v91
	v_rndne_f32_e32 v93, v91
	v_fmamk_f32 v92, v90, 0x32a5705f, v92
	v_sub_f32_e32 v91, v91, v93
	v_add_f32_e32 v91, v91, v92
	v_exp_f32_e32 v91, v91
	v_cvt_i32_f32_e32 v92, v93
	s_mov_b32 s3, 0xc2ce8ed0
	v_cmp_ngt_f32_e32 vcc, s3, v90
	s_mov_b32 s3, 0x42b17218
	v_ldexp_f32 v91, v91, v92
	v_cndmask_b32_e32 v91, 0, v91, vcc
	v_mov_b32_e32 v92, 0x7f800000
	v_cmp_nlt_f32_e32 vcc, s3, v90
	s_mov_b32 s3, 0xbfb8aa3b
	s_nop 1
	v_cndmask_b32_e32 v90, v92, v91, vcc
	v_mov_b32_e32 v93, 0
	s_nop 0
	v_fma_mixlo_f16 v93, v90, s3, 0
	v_and_b32_e32 v28, 0xffff, v93
	v_mov_b32_e32 v29, 0
	v_mov_b32_e32 v30, 0
	v_mov_b32_e32 v31, 0
	v_mov_b32_e32 v32, 0
	v_mov_b32_e32 v33, 0
	v_mov_b32_e32 v34, 0
	v_mov_b32_e32 v35, 0
	v_mov_b32_e32 v96, 0x1c00
	v_mov_b32_e32 v97, 0x1c000000
	v_cmp_eq_u32_e32 vcc, 0, v89
	s_nop 1
	v_cndmask_b32_e32 v20, 0, v96, vcc
	v_cmp_eq_u32_e32 vcc, 1, v89
	s_nop 1
	v_cndmask_b32_e32 v20, v20, v97, vcc
	v_cmp_eq_u32_e32 vcc, 2, v89
	s_nop 1
	v_cndmask_b32_e32 v21, 0, v96, vcc
	v_cmp_eq_u32_e32 vcc, 3, v89
	s_nop 1
	v_cndmask_b32_e32 v21, v21, v97, vcc
	v_cmp_eq_u32_e32 vcc, 4, v89
	s_nop 1
	v_cndmask_b32_e32 v22, 0, v96, vcc
	v_cmp_eq_u32_e32 vcc, 5, v89
	s_nop 1
	v_cndmask_b32_e32 v22, v22, v97, vcc
	v_cmp_eq_u32_e32 vcc, 6, v89
	s_nop 1
	v_cndmask_b32_e32 v23, 0, v96, vcc
	v_cmp_eq_u32_e32 vcc, 7, v89
	s_nop 1
	v_cndmask_b32_e32 v23, v23, v97, vcc
	v_cmp_eq_u32_e32 vcc, 8, v89
	s_nop 1
	v_cndmask_b32_e32 v24, 0, v96, vcc
	v_cmp_eq_u32_e32 vcc, 9, v89
	s_nop 1
	v_cndmask_b32_e32 v24, v24, v97, vcc
	v_cmp_eq_u32_e32 vcc, 10, v89
	s_nop 1
	v_cndmask_b32_e32 v25, 0, v96, vcc
	v_cmp_eq_u32_e32 vcc, 11, v89
	s_nop 1
	v_cndmask_b32_e32 v25, v25, v97, vcc
	v_cmp_eq_u32_e32 vcc, 12, v89
	s_nop 1
	v_cndmask_b32_e32 v26, 0, v96, vcc
	v_cmp_eq_u32_e32 vcc, 13, v89
	s_nop 1
	v_cndmask_b32_e32 v26, v26, v97, vcc
	v_cmp_eq_u32_e32 vcc, 14, v89
	s_nop 1
	v_cndmask_b32_e32 v27, 0, v96, vcc
	v_cmp_eq_u32_e32 vcc, 15, v89
	s_nop 1
	v_cndmask_b32_e32 v27, v27, v97, vcc
	v_mov_b32_e32 v195, 0
	v_mov_b32_e32 v85, 0
	v_mov_b32_e32 v88, 0
	v_mov_b32_e32 v84, 0
	v_mov_b32_e32 v68, 0
	v_mov_b32_e32 v69, 0
	v_mov_b32_e32 v70, 0
	v_mov_b32_e32 v71, 0
	v_mov_b32_e32 v72, 0
	v_mov_b32_e32 v73, 0
	v_mov_b32_e32 v74, 0
	v_mov_b32_e32 v75, 0
	v_mov_b32_e32 v76, 0
	v_mov_b32_e32 v77, 0
	v_mov_b32_e32 v78, 0
	v_mov_b32_e32 v79, 0
	v_mov_b32_e32 v80, 0
	v_mov_b32_e32 v81, 0
	v_mov_b32_e32 v82, 0
	v_mov_b32_e32 v83, 0
	s_waitcnt vmcnt(18)
	v_add_u32_e32 v8, 0x200, v8
	v_add_u32_e32 v94, 0x800, v8
	v_mov_b32_e32 v92, v2
	v_add_u32_e32 v93, 0x4000, v2
	s_mov_b32 s29, s28
	ds_write_b16 v8, v18
	ds_write_b16 v8, v19 offset:1024
	s_add_u32 s26, s26, 0x100
	s_addc_u32 s27, s27, 0
	global_load_ushort v18, v7, s[26:27]
	global_load_ushort v19, v7, s[26:27] offset:128
	s_add_u32 s26, s26, 0x100
	s_addc_u32 s27, s27, 0
	s_waitcnt vmcnt(0)
	s_waitcnt lgkmcnt(0)
	s_barrier
	ds_read_b128 v[52:55], v92 offset:32768
	ds_read_b128 v[56:59], v92 offset:33792
	ds_read_u16 v32, v9 offset:0
	ds_read_b128 v[36:39], v11 offset:0
	ds_read_b128 v[44:47], v92 offset:0
	ds_read_b128 v[48:51], v92 offset:1024
	s_waitcnt lgkmcnt(0)
	v_mfma_f32_32x32x16_f16 v[98:113], v[32:35], v[28:31], 0
	v_mfma_f32_32x32x16_f16 v[132:147], v[36:39], v[44:47], 0
	v_mfma_f32_32x32x16_f16 v[164:179], v[36:39], v[48:51], 0
	ds_read_u16 v32, v9 offset:32
	ds_read_b128 v[36:39], v11 offset:256
	ds_read_b128 v[44:47], v92 offset:2048
	ds_read_b128 v[48:51], v92 offset:3072
	s_nop 15
	s_nop 15
	s_waitcnt lgkmcnt(0)
